# moe2 main loop: LDS-DMA pieces rebalanced 2/6/2/6 to 4/4/4/4 per sub-phase, vmcnt recounted
# baseline (speedup 1.0000x reference)
; #define PG8_STAGE(bufoff, gbase, v0, v1) do { glds16_s((gbase), (v0), ldsbase + (unsigned)(bufoff)); glds16_s((gbase), (v1), ldsbase + (unsigned)(bufoff) + 8192u); } while (0)
; #define PG8_LDA(dst, b, h) do { _Pragma("unroll") for (int m = 0; m < 4; ++m) _Pragma("unroll") for (int k = 0; k < 2; ++k) dst[m][k] = *(const LAS bf16x8*)(lds + PG8_SA(b, h) + aoff + m * 2048 + k * 1024); } while (0)
; #define PG8_LDB(dst, b, h) do { _Pragma("unroll") for (int n = 0; n < 2; ++n) _Pragma("unroll") for (int k = 0; k < 2; ++k) dst[n][k] = *(const LAS bf16x8*)(lds + PG8_SB(b, h) + boff + n * 2048 + k * 1024); } while (0)
; #define PG8_WAIT_V(n) asm volatile("s_waitcnt vmcnt(" #n ")" ::: "memory")
; #define PG8_WAIT_L(n) asm volatile("s_waitcnt lgkmcnt(" #n ")" ::: "memory")
; #define PG8_BAR __builtin_amdgcn_s_barrier()
; #define PG8_SCHED __builtin_amdgcn_sched_barrier(0)
; template <class Epi, class Sched, bool ALIGN_EPI, bool FP8 = false>
; __device__ __forceinline__ void gemm_phase(LAS unsigned char* lds, const bf16_t* A, const bf16_t* Bt, const int K, const Sched& S, const Epi& E, const int wave_in) {
;     ...
;             const unsigned w00 = last ? vN[0][0] : vA[0][0], w01 = last ? vN[0][1] : vA[0][1], w10 = last ? vN[1][0] : vA[1][0], w11 = last ? vN[1][1] : vA[1][1];
;             PG8_LDB(B0, 0, 0); PG8_LDB(B1, 0, 1); PG8_SCHED; PG8_LDA(At, 0, 0); PG8_STAGE(PG8_SA(1, 1), a1, vA[1][0], vA[1][1]);
;             PG8_WAIT_V(8); PG8_WAIT_L(0); PG8_BAR; PG8_MMA(0, 0, At, B0); PG8_MMA(0, 1, At, B1); PG8_BAR; PG8_SCHED;
;             PG8_LDA(At, 0, 1); PG8_STAGE(PG8_SB(0, 0), b2, voffB[0], voffB[1]); PG8_STAGE(PG8_SB(0, 1), b2 + hstep, voffB[0], voffB[1]); PG8_STAGE(PG8_SA(0, 0), a2, w00, w01);
;             PG8_WAIT_V(8); PG8_WAIT_L(0); PG8_BAR; PG8_MMA(1, 0, At, B0); PG8_MMA(1, 1, At, B1); PG8_BAR; PG8_SCHED;
.LBB0_1139:
	s_add_u32 s60, s14, 0x100
	s_addc_u32 s61, s15, 0
	v_add_u32_e32 v2, 0x10000, v169
	v_add_u32_e32 v6, 0x14000, v169
	s_cmp_eq_u32 s89, 4
	ds_read_b128 v[26:29], v2
	ds_read_b128 v[30:33], v2 offset:1024
	ds_read_b128 v[18:21], v2 offset:2048
	ds_read_b128 v[22:25], v2 offset:3072
	ds_read_b128 v[10:13], v6
	ds_read_b128 v[14:17], v6 offset:1024
	ds_read_b128 v[2:5], v6 offset:2048
	ds_read_b128 v[6:9], v6 offset:3072
	s_cselect_b64 vcc, -1, 0
	s_and_b64 s[10:11], vcc, exec
	s_cselect_b32 s92, s76, s60
	s_cselect_b32 s93, s77, s61
	s_cselect_b32 s16, s4, s0
	s_cselect_b32 s17, s5, s1
	s_add_u32 s10, s92, 0x80
	s_addc_u32 s11, s93, 0
	s_add_u32 s12, s14, 0x80
	v_cndmask_b32_e32 v179, v175, v171, vcc
	v_cndmask_b32_e32 v181, v178, v173, vcc
	s_addc_u32 s13, s15, 0
	v_cndmask_b32_e32 v180, v176, v172, vcc
	ds_read_b128 v[198:201], v170
	ds_read_b128 v[202:205], v170 offset:1024
	ds_read_b128 v[206:209], v170 offset:2048
	ds_read_b128 v[210:213], v170 offset:3072
	ds_read_b128 v[214:217], v170 offset:4096
	ds_read_b128 v[218:221], v170 offset:5120
	ds_read_b128 v[222:225], v170 offset:6144
	ds_read_b128 v[226:229], v170 offset:7168
	s_mov_b32 s31, m0
	s_mov_b32 m0, s65
	s_nop 0
	global_load_lds_dwordx4 v178, s[12:13]
	s_mov_b32 m0, s31
	s_add_u32 s14, s16, 0x80
	s_mov_b32 s31, m0
	s_mov_b32 m0, s66
	s_nop 0
	global_load_lds_dwordx4 v177, s[12:13]
	s_mov_b32 m0, s31
	s_mov_b32 s31, m0
	s_mov_b32 m0, s57
	s_nop 0
	global_load_lds_dwordx4 v175, s[12:13]
	s_mov_b32 m0, s31
	s_nop 0
	s_mov_b32 s31, m0
	s_mov_b32 m0, s58
	s_nop 0
	global_load_lds_dwordx4 v176, s[12:13]
	s_mov_b32 m0, s31
	s_waitcnt vmcnt(10)
	s_waitcnt lgkmcnt(0)
	s_addc_u32 s15, s17, 0
	s_barrier
	s_setprio 1
	s_waitcnt lgkmcnt(6)
	v_mfma_scale_f32_16x16x128_f8f6f4 v[160:163], v[26:33], v[198:205], v[160:163], v186, v187 op_sel_hi:[0,0,0]
	v_mfma_scale_f32_16x16x128_f8f6f4 v[156:159], v[18:25], v[198:205], v[156:159], v186, v187 op_sel_hi:[0,0,0]
	s_waitcnt lgkmcnt(4)
	v_mfma_scale_f32_16x16x128_f8f6f4 v[142:145], v[26:33], v[206:213], v[142:145], v186, v187 op_sel_hi:[0,0,0]
	v_mfma_scale_f32_16x16x128_f8f6f4 v[138:141], v[18:25], v[206:213], v[138:141], v186, v187 op_sel_hi:[0,0,0]
	s_waitcnt lgkmcnt(2)
	v_mfma_scale_f32_16x16x128_f8f6f4 v[126:129], v[26:33], v[214:221], v[126:129], v186, v187 op_sel_hi:[0,0,0]
	v_mfma_scale_f32_16x16x128_f8f6f4 v[122:125], v[18:25], v[214:221], v[122:125], v186, v187 op_sel_hi:[0,0,0]
	s_waitcnt lgkmcnt(0)
	v_mfma_scale_f32_16x16x128_f8f6f4 v[110:113], v[26:33], v[222:229], v[110:113], v186, v187 op_sel_hi:[0,0,0]
	v_mfma_scale_f32_16x16x128_f8f6f4 v[106:109], v[18:25], v[222:229], v[106:109], v186, v187 op_sel_hi:[0,0,0]
	s_setprio 0
	s_setprio 1
	v_mfma_scale_f32_16x16x128_f8f6f4 v[152:155], v[10:17], v[198:205], v[152:155], v186, v187 op_sel_hi:[0,0,0]
	v_mfma_scale_f32_16x16x128_f8f6f4 v[148:151], v[2:9], v[198:205], v[148:151], v186, v187 op_sel_hi:[0,0,0]
	v_mfma_scale_f32_16x16x128_f8f6f4 v[134:137], v[10:17], v[206:213], v[134:137], v186, v187 op_sel_hi:[0,0,0]
	v_mfma_scale_f32_16x16x128_f8f6f4 v[130:133], v[2:9], v[206:213], v[130:133], v186, v187 op_sel_hi:[0,0,0]
	v_mfma_scale_f32_16x16x128_f8f6f4 v[118:121], v[10:17], v[214:221], v[118:121], v186, v187 op_sel_hi:[0,0,0]
	v_mfma_scale_f32_16x16x128_f8f6f4 v[114:117], v[2:9], v[214:221], v[114:117], v186, v187 op_sel_hi:[0,0,0]
	v_mfma_scale_f32_16x16x128_f8f6f4 v[102:105], v[10:17], v[222:229], v[102:105], v186, v187 op_sel_hi:[0,0,0]
	v_mfma_scale_f32_16x16x128_f8f6f4 v[98:101], v[2:9], v[222:229], v[98:101], v186, v187 op_sel_hi:[0,0,0]
	s_setprio 0
	s_barrier
	ds_read_b128 v[198:201], v170 offset:16384
	ds_read_b128 v[202:205], v170 offset:17408
	ds_read_b128 v[206:209], v170 offset:18432
	ds_read_b128 v[210:213], v170 offset:19456
	ds_read_b128 v[214:217], v170 offset:20480
	ds_read_b128 v[218:221], v170 offset:21504
	ds_read_b128 v[222:225], v170 offset:22528
	ds_read_b128 v[226:229], v170 offset:23552
	s_mov_b32 s12, m0
	s_mov_b32 m0, s27
	s_nop 0
	global_load_lds_dwordx4 v0, s[16:17]
	s_mov_b32 m0, s12
	s_nop 0
	s_mov_b32 s12, m0
	s_mov_b32 m0, s48
	s_nop 0
	global_load_lds_dwordx4 v147, s[16:17]
	s_mov_b32 m0, s12
	s_add_u32 s12, s16, 0x20000
	s_addc_u32 s13, s17, 0
	s_mov_b32 s31, m0
	s_mov_b32 m0, s49
	s_nop 0
	global_load_lds_dwordx4 v0, s[12:13]
	s_mov_b32 m0, s31
	s_nop 0
	s_mov_b32 s31, m0
	s_mov_b32 m0, s50
	s_nop 0
	global_load_lds_dwordx4 v147, s[12:13]
	s_mov_b32 m0, s31
	s_waitcnt vmcnt(4)
	s_waitcnt lgkmcnt(0)
	s_barrier
	s_setprio 1
	s_waitcnt lgkmcnt(6)
	v_mfma_scale_f32_16x16x128_f8f6f4 v[94:97], v[26:33], v[198:205], v[94:97], v186, v187 op_sel_hi:[0,0,0]
	v_mfma_scale_f32_16x16x128_f8f6f4 v[90:93], v[18:25], v[198:205], v[90:93], v186, v187 op_sel_hi:[0,0,0]
	s_waitcnt lgkmcnt(4)
	v_mfma_scale_f32_16x16x128_f8f6f4 v[78:81], v[26:33], v[206:213], v[78:81], v186, v187 op_sel_hi:[0,0,0]
	v_mfma_scale_f32_16x16x128_f8f6f4 v[74:77], v[18:25], v[206:213], v[74:77], v186, v187 op_sel_hi:[0,0,0]
	s_waitcnt lgkmcnt(2)
	v_mfma_scale_f32_16x16x128_f8f6f4 v[62:65], v[26:33], v[214:221], v[62:65], v186, v187 op_sel_hi:[0,0,0]
	v_mfma_scale_f32_16x16x128_f8f6f4 v[58:61], v[18:25], v[214:221], v[58:61], v186, v187 op_sel_hi:[0,0,0]
	s_waitcnt lgkmcnt(0)
	v_mfma_scale_f32_16x16x128_f8f6f4 v[46:49], v[26:33], v[222:229], v[46:49], v186, v187 op_sel_hi:[0,0,0]
	v_mfma_scale_f32_16x16x128_f8f6f4 v[42:45], v[18:25], v[222:229], v[42:45], v186, v187 op_sel_hi:[0,0,0]
	s_setprio 0
	s_setprio 1
	v_mfma_scale_f32_16x16x128_f8f6f4 v[86:89], v[10:17], v[198:205], v[86:89], v186, v187 op_sel_hi:[0,0,0]
	v_mfma_scale_f32_16x16x128_f8f6f4 v[82:85], v[2:9], v[198:205], v[82:85], v186, v187 op_sel_hi:[0,0,0]
	v_mfma_scale_f32_16x16x128_f8f6f4 v[70:73], v[10:17], v[206:213], v[70:73], v186, v187 op_sel_hi:[0,0,0]
	v_mfma_scale_f32_16x16x128_f8f6f4 v[66:69], v[2:9], v[206:213], v[66:69], v186, v187 op_sel_hi:[0,0,0]
	v_mfma_scale_f32_16x16x128_f8f6f4 v[54:57], v[10:17], v[214:221], v[54:57], v186, v187 op_sel_hi:[0,0,0]
	v_mfma_scale_f32_16x16x128_f8f6f4 v[50:53], v[2:9], v[214:221], v[50:53], v186, v187 op_sel_hi:[0,0,0]
	v_mfma_scale_f32_16x16x128_f8f6f4 v[38:41], v[10:17], v[222:229], v[38:41], v186, v187 op_sel_hi:[0,0,0]
	v_mfma_scale_f32_16x16x128_f8f6f4 v[34:37], v[2:9], v[222:229], v[34:37], v186, v187 op_sel_hi:[0,0,0]
	s_setprio 0
	s_barrier
; #define PG8_STAGE(bufoff, gbase, v0, v1) do { glds16_s((gbase), (v0), ldsbase + (unsigned)(bufoff)); glds16_s((gbase), (v1), ldsbase + (unsigned)(bufoff) + 8192u); } while (0)
; #define PG8_LDA(dst, b, h) do { _Pragma("unroll") for (int m = 0; m < 4; ++m) _Pragma("unroll") for (int k = 0; k < 2; ++k) dst[m][k] = *(const LAS bf16x8*)(lds + PG8_SA(b, h) + aoff + m * 2048 + k * 1024); } while (0)
; #define PG8_LDB(dst, b, h) do { _Pragma("unroll") for (int n = 0; n < 2; ++n) _Pragma("unroll") for (int k = 0; k < 2; ++k) dst[n][k] = *(const LAS bf16x8*)(lds + PG8_SB(b, h) + boff + n * 2048 + k * 1024); } while (0)
; #define PG8_WAIT_V(n) asm volatile("s_waitcnt vmcnt(" #n ")" ::: "memory")
; #define PG8_WAIT_L(n) asm volatile("s_waitcnt lgkmcnt(" #n ")" ::: "memory")
; #define PG8_BAR __builtin_amdgcn_s_barrier()
; #define PG8_SCHED __builtin_amdgcn_sched_barrier(0)
; template <class Epi, class Sched, bool ALIGN_EPI, bool FP8 = false>
; __device__ __forceinline__ void gemm_phase(LAS unsigned char* lds, const bf16_t* A, const bf16_t* Bt, const int K, const Sched& S, const Epi& E, const int wave_in) {
;     ...
;             PG8_LDB(B0, 1, 0); PG8_LDB(B1, 1, 1); PG8_SCHED; PG8_LDA(At, 1, 0); PG8_STAGE(PG8_SA(0, 1), a2, w10, w11);
;             PG8_WAIT_V(8); PG8_WAIT_L(0); PG8_BAR; PG8_MMA(0, 0, At, B0); PG8_MMA(0, 1, At, B1); PG8_BAR; PG8_SCHED;
;             PG8_LDA(At, 1, 1); PG8_STAGE(PG8_SB(1, 0), b3, voffB[0], voffB[1]); PG8_STAGE(PG8_SB(1, 1), b3 + hstep, voffB[0], voffB[1]); PG8_STAGE(PG8_SA(1, 0), a3, w00, w01);
;             PG8_WAIT_V(8); PG8_WAIT_L(0); PG8_BAR; PG8_MMA(1, 0, At, B0); PG8_MMA(1, 1, At, B1); PG8_BAR; PG8_SCHED;
;         }
;         if constexpr (FP8) asm volatile("s_nop 15\n\ts_nop 15" ::: "memory");
;         if constexpr (ALIGN_EPI) { if (wr == 0) PG8_BAR; }
	v_add_u32_e32 v14, 0x18000, v169
	v_add_u32_e32 v30, 0x1c000, v169
	ds_read_b128 v[2:5], v14
	ds_read_b128 v[6:9], v14 offset:1024
	ds_read_b128 v[10:13], v14 offset:2048
	ds_read_b128 v[14:17], v14 offset:3072
	ds_read_b128 v[18:21], v30
	ds_read_b128 v[22:25], v30 offset:1024
	ds_read_b128 v[26:29], v30 offset:2048
	ds_read_b128 v[30:33], v30 offset:3072
	ds_read_b128 v[198:201], v170 offset:32768
	ds_read_b128 v[202:205], v170 offset:33792
	ds_read_b128 v[206:209], v170 offset:34816
	ds_read_b128 v[210:213], v170 offset:35840
	ds_read_b128 v[214:217], v170 offset:36864
	ds_read_b128 v[218:221], v170 offset:37888
	ds_read_b128 v[222:225], v170 offset:38912
	ds_read_b128 v[226:229], v170 offset:39936
	s_mov_b32 s12, m0
	s_mov_b32 m0, s52
	s_nop 0
	global_load_lds_dwordx4 v181, s[92:93]
	s_mov_b32 m0, s12
	v_cndmask_b32_e32 v197, v177, v174, vcc
	s_mov_b32 s12, m0
	s_mov_b32 m0, s53
	s_nop 0
	global_load_lds_dwordx4 v197, s[92:93]
	s_mov_b32 m0, s12
	s_mov_b32 s12, m0
	s_mov_b32 m0, s39
	s_nop 0
	global_load_lds_dwordx4 v179, s[92:93]
	s_mov_b32 m0, s12
	s_nop 0
	s_mov_b32 s12, m0
	s_mov_b32 m0, s51
	s_nop 0
	global_load_lds_dwordx4 v180, s[92:93]
	s_mov_b32 m0, s12
	s_waitcnt vmcnt(10)
	s_waitcnt lgkmcnt(0)
	s_barrier
	s_setprio 1
	s_waitcnt lgkmcnt(6)
	v_mfma_scale_f32_16x16x128_f8f6f4 v[160:163], v[2:9], v[198:205], v[160:163], v186, v187 op_sel_hi:[0,0,0]
	v_mfma_scale_f32_16x16x128_f8f6f4 v[156:159], v[10:17], v[198:205], v[156:159], v186, v187 op_sel_hi:[0,0,0]
	s_waitcnt lgkmcnt(4)
	v_mfma_scale_f32_16x16x128_f8f6f4 v[142:145], v[2:9], v[206:213], v[142:145], v186, v187 op_sel_hi:[0,0,0]
	v_mfma_scale_f32_16x16x128_f8f6f4 v[138:141], v[10:17], v[206:213], v[138:141], v186, v187 op_sel_hi:[0,0,0]
	s_waitcnt lgkmcnt(2)
	v_mfma_scale_f32_16x16x128_f8f6f4 v[126:129], v[2:9], v[214:221], v[126:129], v186, v187 op_sel_hi:[0,0,0]
	v_mfma_scale_f32_16x16x128_f8f6f4 v[122:125], v[10:17], v[214:221], v[122:125], v186, v187 op_sel_hi:[0,0,0]
	s_waitcnt lgkmcnt(0)
	v_mfma_scale_f32_16x16x128_f8f6f4 v[110:113], v[2:9], v[222:229], v[110:113], v186, v187 op_sel_hi:[0,0,0]
	v_mfma_scale_f32_16x16x128_f8f6f4 v[106:109], v[10:17], v[222:229], v[106:109], v186, v187 op_sel_hi:[0,0,0]
	s_setprio 0
	s_setprio 1
	v_mfma_scale_f32_16x16x128_f8f6f4 v[152:155], v[18:25], v[198:205], v[152:155], v186, v187 op_sel_hi:[0,0,0]
	v_mfma_scale_f32_16x16x128_f8f6f4 v[148:151], v[26:33], v[198:205], v[148:151], v186, v187 op_sel_hi:[0,0,0]
	v_mfma_scale_f32_16x16x128_f8f6f4 v[134:137], v[18:25], v[206:213], v[134:137], v186, v187 op_sel_hi:[0,0,0]
	v_mfma_scale_f32_16x16x128_f8f6f4 v[130:133], v[26:33], v[206:213], v[130:133], v186, v187 op_sel_hi:[0,0,0]
	v_mfma_scale_f32_16x16x128_f8f6f4 v[118:121], v[18:25], v[214:221], v[118:121], v186, v187 op_sel_hi:[0,0,0]
	v_mfma_scale_f32_16x16x128_f8f6f4 v[114:117], v[26:33], v[214:221], v[114:117], v186, v187 op_sel_hi:[0,0,0]
	v_mfma_scale_f32_16x16x128_f8f6f4 v[102:105], v[18:25], v[222:229], v[102:105], v186, v187 op_sel_hi:[0,0,0]
	v_mfma_scale_f32_16x16x128_f8f6f4 v[98:101], v[26:33], v[222:229], v[98:101], v186, v187 op_sel_hi:[0,0,0]
	s_setprio 0
	s_barrier
	ds_read_b128 v[198:201], v170 offset:49152
	ds_read_b128 v[202:205], v170 offset:50176
	ds_read_b128 v[206:209], v170 offset:51200
	ds_read_b128 v[210:213], v170 offset:52224
	ds_read_b128 v[214:217], v170 offset:53248
	ds_read_b128 v[218:221], v170 offset:54272
	ds_read_b128 v[222:225], v170 offset:55296
	ds_read_b128 v[226:229], v170 offset:56320
	s_mov_b32 s12, m0
	s_mov_b32 m0, s55
	s_nop 0
	global_load_lds_dwordx4 v0, s[14:15]
	s_mov_b32 m0, s12
	s_nop 0
	s_mov_b32 s12, m0
	s_mov_b32 m0, s56
	s_nop 0
	global_load_lds_dwordx4 v147, s[14:15]
	s_mov_b32 m0, s12
	s_add_u32 s12, s16, 0x20080
	s_addc_u32 s13, s17, 0
	s_mov_b32 s14, m0
	s_mov_b32 m0, s59
	s_nop 0
	global_load_lds_dwordx4 v0, s[12:13]
	s_mov_b32 m0, s14
	s_nop 0
	s_mov_b32 s14, m0
	s_mov_b32 m0, s64
	s_nop 0
	global_load_lds_dwordx4 v147, s[12:13]
	s_mov_b32 m0, s14
	s_waitcnt vmcnt(4)
	s_waitcnt lgkmcnt(0)
	s_barrier
	s_setprio 1
	s_waitcnt lgkmcnt(6)
	v_mfma_scale_f32_16x16x128_f8f6f4 v[94:97], v[2:9], v[198:205], v[94:97], v186, v187 op_sel_hi:[0,0,0]
	v_mfma_scale_f32_16x16x128_f8f6f4 v[90:93], v[10:17], v[198:205], v[90:93], v186, v187 op_sel_hi:[0,0,0]
	s_waitcnt lgkmcnt(4)
	v_mfma_scale_f32_16x16x128_f8f6f4 v[78:81], v[2:9], v[206:213], v[78:81], v186, v187 op_sel_hi:[0,0,0]
	v_mfma_scale_f32_16x16x128_f8f6f4 v[74:77], v[10:17], v[206:213], v[74:77], v186, v187 op_sel_hi:[0,0,0]
	s_waitcnt lgkmcnt(2)
	v_mfma_scale_f32_16x16x128_f8f6f4 v[62:65], v[2:9], v[214:221], v[62:65], v186, v187 op_sel_hi:[0,0,0]
	v_mfma_scale_f32_16x16x128_f8f6f4 v[58:61], v[10:17], v[214:221], v[58:61], v186, v187 op_sel_hi:[0,0,0]
	s_waitcnt lgkmcnt(0)
	v_mfma_scale_f32_16x16x128_f8f6f4 v[46:49], v[2:9], v[222:229], v[46:49], v186, v187 op_sel_hi:[0,0,0]
	v_mfma_scale_f32_16x16x128_f8f6f4 v[42:45], v[10:17], v[222:229], v[42:45], v186, v187 op_sel_hi:[0,0,0]
	s_setprio 0
	s_setprio 1
	v_mfma_scale_f32_16x16x128_f8f6f4 v[86:89], v[18:25], v[198:205], v[86:89], v186, v187 op_sel_hi:[0,0,0]
	v_mfma_scale_f32_16x16x128_f8f6f4 v[82:85], v[26:33], v[198:205], v[82:85], v186, v187 op_sel_hi:[0,0,0]
	v_mfma_scale_f32_16x16x128_f8f6f4 v[70:73], v[18:25], v[206:213], v[70:73], v186, v187 op_sel_hi:[0,0,0]
	v_mfma_scale_f32_16x16x128_f8f6f4 v[66:69], v[26:33], v[206:213], v[66:69], v186, v187 op_sel_hi:[0,0,0]
	v_mfma_scale_f32_16x16x128_f8f6f4 v[54:57], v[18:25], v[214:221], v[54:57], v186, v187 op_sel_hi:[0,0,0]
	v_mfma_scale_f32_16x16x128_f8f6f4 v[50:53], v[26:33], v[214:221], v[50:53], v186, v187 op_sel_hi:[0,0,0]
	v_mfma_scale_f32_16x16x128_f8f6f4 v[38:41], v[18:25], v[222:229], v[38:41], v186, v187 op_sel_hi:[0,0,0]
	v_mfma_scale_f32_16x16x128_f8f6f4 v[34:37], v[26:33], v[222:229], v[34:37], v186, v187 op_sel_hi:[0,0,0]
	s_setprio 0
	s_barrier
	s_add_i32 s89, s89, 2
	s_add_u32 s0, s0, 0x100
	s_addc_u32 s1, s1, 0
	s_cmp_gt_u32 s89, 5
	s_mov_b64 s[14:15], s[60:61]
	s_cbranch_scc0 .LBB0_1139
	s_nop 15
	s_nop 15
	s_and_b64 vcc, exec, s[86:87]
	s_cbranch_vccz .LBB0_1142
	s_barrier
